# s8 + mask blocks leave early (s_cbranch_execz) when no lane masks the tile's largest key
# baseline (speedup 1.0000x reference)
; __device__ __forceinline__ void cmask(f32x16& p0, f32x16& p1, int jb, int qrel, int hi) {
;     const float NEG = -INFINITY; int kb = 64 * jb + 4 * hi;
; #pragma unroll
;     for (int r = 0; r < 16; ++r) { int kv = kb + (r & 3) + 8 * (r >> 2); if (kv > qrel) p0[r] = NEG; if (kv + 32 > qrel) p1[r] = NEG; }
; }
.LBB0_477:
	v_add_u32_e32 v184, s0, v230
	ds_read_b64_tr_b16 v[180:181], v184 offset:24576
	ds_read_b64_tr_b16 v[182:183], v184 offset:25088
	s_waitcnt lgkmcnt(9)
	v_mfma_f32_32x32x16_f16 v[48:63], v[176:179], v[128:131], v[48:63]
	v_add_f32_e32 v132, v80, v81
	v_add_f32_e32 v132, v82, v132
	v_add_f32_e32 v132, v83, v132
	v_add_f32_e32 v132, v84, v132
	v_add_f32_e32 v132, v85, v132
	v_cvt_pk_f16_f32 v144, v80, v81
	v_cvt_pk_f16_f32 v145, v82, v83
	ds_read_b64_tr_b16 v[176:177], v184 offset:28672
	ds_read_b64_tr_b16 v[178:179], v184 offset:29184
	s_waitcnt lgkmcnt(10)
	v_mfma_f32_32x32x16_f16 v[32:47], v[172:175], v[128:131], v[32:47]
	v_add_f32_e32 v80, v86, v132
	v_add_f32_e32 v80, v87, v80
	v_add_f32_e32 v80, v88, v80
	v_add_f32_e32 v80, v89, v80
	v_cvt_pk_f16_f32 v146, v84, v85
	v_cvt_pk_f16_f32 v147, v86, v87
	ds_read_b64_tr_b16 v[172:173], v184 offset:25600
	ds_read_b64_tr_b16 v[174:175], v184 offset:26112
	s_waitcnt lgkmcnt(11)
	v_mfma_f32_32x32x16_f16 v[48:63], v[168:171], v[124:127], v[48:63]
	v_add_f32_e32 v80, v90, v80
	v_add_f32_e32 v80, v91, v80
	v_add_f32_e32 v80, v92, v80
	v_add_f32_e32 v80, v93, v80
	v_cvt_pk_f16_f32 v140, v88, v89
	v_cvt_pk_f16_f32 v141, v90, v91
	ds_read_b64_tr_b16 v[84:85], v184 offset:29696
	ds_read_b64_tr_b16 v[86:87], v184 offset:30208
	s_waitcnt lgkmcnt(12)
	v_mfma_f32_32x32x16_f16 v[32:47], v[164:167], v[124:127], v[32:47]
	v_add_f32_e32 v80, v94, v80
	v_add_f32_e32 v80, v95, v80
	v_add_f32_e32 v80, v64, v80
	v_add_f32_e32 v88, v65, v80
	v_cvt_pk_f16_f32 v142, v92, v93
	v_cvt_pk_f16_f32 v143, v94, v95
	ds_read_b64_tr_b16 v[80:81], v184 offset:26624
	ds_read_b64_tr_b16 v[82:83], v184 offset:27136
	s_waitcnt lgkmcnt(13)
	v_mfma_f32_32x32x16_f16 v[48:63], v[160:163], v[120:123], v[48:63]
	v_add_f32_e32 v88, v66, v88
	v_add_f32_e32 v88, v67, v88
	v_add_f32_e32 v88, v68, v88
	v_add_f32_e32 v88, v69, v88
	v_cvt_pk_f16_f32 v136, v64, v65
	v_cvt_pk_f16_f32 v137, v66, v67
	ds_read_b64_tr_b16 v[160:161], v184 offset:30720
	ds_read_b64_tr_b16 v[162:163], v184 offset:31232
	s_waitcnt lgkmcnt(14)
	v_mfma_f32_32x32x16_f16 v[32:47], v[152:155], v[120:123], v[32:47]
	v_add_f32_e32 v64, v70, v88
	v_add_f32_e32 v64, v71, v64
	v_add_f32_e32 v64, v72, v64
	v_add_f32_e32 v88, v73, v64
	v_cvt_pk_f16_f32 v138, v68, v69
	v_cvt_pk_f16_f32 v139, v70, v71
	ds_read_b64_tr_b16 v[64:65], v184 offset:27648
	ds_read_b64_tr_b16 v[66:67], v184 offset:28160
	s_waitcnt lgkmcnt(14)
	v_mfma_f32_32x32x16_f16 v[48:63], v[156:159], v[116:119], v[48:63]
	v_add_f32_e32 v68, v74, v88
	v_add_f32_e32 v68, v75, v68
	v_add_f32_e32 v68, v76, v68
	v_add_f32_e32 v68, v77, v68
	v_cvt_pk_f16_f32 v132, v72, v73
	v_cvt_pk_f16_f32 v133, v74, v75
	ds_read_b64_tr_b16 v[152:153], v184 offset:31744
	ds_read_b64_tr_b16 v[154:155], v184 offset:32256
	v_mfma_f32_32x32x16_f16 v[32:47], v[148:151], v[116:119], v[32:47]
	v_add_f32_e32 v68, v78, v68
	v_add_f32_e32 v68, v79, v68
	v_add_f32_e32 v68, 0, v68
	v_cvt_pk_f16_f32 v134, v76, v77
	v_cvt_pk_f16_f32 v135, v78, v79
	s_add_i32 s0, s70, s89
	s_cmp_lt_u32 s69, 3
	s_cselect_b64 s[40:41], -1, 0
	s_mov_b32 s1, m0
	s_mov_b32 m0, s0
	s_nop 0
	global_load_lds_dwordx4 v[194:195], off
	s_mov_b32 m0, s1
	s_and_b64 s[0:1], s[40:41], exec
	s_cselect_b32 s18, s50, -3
	s_add_i32 s18, s18, s69
	v_mad_i64_i32 v[70:71], s[0:1], s18, v249, v[216:217]
	s_add_i32 s0, s68, s36
	s_mov_b32 s1, m0
	s_mov_b32 m0, s0
	s_nop 0
	global_load_lds_dwordx4 v[70:71], off
	s_mov_b32 m0, s1
	s_cmp_gt_u32 s69, 3
	s_cbranch_scc1 .LBB0_479
	s_mov_b64 s[100:101], exec
	v_sub_u32_e32 v70, v215, v197
	v_add_u32_e32 v70, 0x7b, v70
	v_cmpx_gt_i32_e32 59, v70
	s_nop 3
	s_cbranch_execz .Lmaskx_done_9
	v_mov_b32_e32 v47, v248
	v_cmpx_gt_i32_e32 58, v70
	v_mov_b32_e32 v46, v248
	v_cmpx_gt_i32_e32 57, v70
	v_mov_b32_e32 v45, v248
	v_cmpx_gt_i32_e32 56, v70
	v_mov_b32_e32 v44, v248
	v_cmpx_gt_i32_e32 51, v70
	v_mov_b32_e32 v43, v248
	v_cmpx_gt_i32_e32 50, v70
	v_mov_b32_e32 v42, v248
	v_cmpx_gt_i32_e32 49, v70
	v_mov_b32_e32 v41, v248
	v_cmpx_gt_i32_e32 48, v70
	v_mov_b32_e32 v40, v248
	v_cmpx_gt_i32_e32 43, v70
	v_mov_b32_e32 v39, v248
	v_cmpx_gt_i32_e32 42, v70
	v_mov_b32_e32 v38, v248
	v_cmpx_gt_i32_e32 41, v70
	v_mov_b32_e32 v37, v248
	v_cmpx_gt_i32_e32 40, v70
	v_mov_b32_e32 v36, v248
	v_cmpx_gt_i32_e32 35, v70
	v_mov_b32_e32 v35, v248
	v_cmpx_gt_i32_e32 34, v70
	v_mov_b32_e32 v34, v248
	v_cmpx_gt_i32_e32 33, v70
	v_mov_b32_e32 v33, v248
	v_cmpx_gt_i32_e32 32, v70
	v_mov_b32_e32 v32, v248
	v_cmpx_gt_i32_e32 27, v70
	v_mov_b32_e32 v63, v248
	v_cmpx_gt_i32_e32 26, v70
	v_mov_b32_e32 v62, v248
	v_cmpx_gt_i32_e32 25, v70
	v_mov_b32_e32 v61, v248
	v_cmpx_gt_i32_e32 24, v70
	v_mov_b32_e32 v60, v248
	v_cmpx_gt_i32_e32 19, v70
	v_mov_b32_e32 v59, v248
	v_cmpx_gt_i32_e32 18, v70
	v_mov_b32_e32 v58, v248
	v_cmpx_gt_i32_e32 17, v70
	v_mov_b32_e32 v57, v248
	v_cmpx_gt_i32_e32 16, v70
	v_mov_b32_e32 v56, v248
	v_cmpx_gt_i32_e32 11, v70
	v_mov_b32_e32 v55, v248
	v_cmpx_gt_i32_e32 10, v70
	v_mov_b32_e32 v54, v248
	v_cmpx_gt_i32_e32 9, v70
	v_mov_b32_e32 v53, v248
	v_cmpx_gt_i32_e32 8, v70
	v_mov_b32_e32 v52, v248
	v_cmpx_gt_i32_e32 3, v70
	v_mov_b32_e32 v51, v248
	v_cmpx_gt_i32_e32 2, v70
	v_mov_b32_e32 v50, v248
	v_cmpx_gt_i32_e32 1, v70
	v_mov_b32_e32 v49, v248
	v_cmpx_gt_i32_e32 0, v70
	v_mov_b32_e32 v48, v248
.Lmaskx_done_9:
	s_mov_b64 exec, s[100:101]
	s_nop 4

; __device__ __forceinline__ void cmask(f32x16& p0, f32x16& p1, int jb, int qrel, int hi) {
;     const float NEG = -INFINITY; int kb = 64 * jb + 4 * hi;
; #pragma unroll
;     for (int r = 0; r < 16; ++r) { int kv = kb + (r & 3) + 8 * (r >> 2); if (kv > qrel) p0[r] = NEG; if (kv + 32 > qrel) p1[r] = NEG; }
; }
.LBB0_482:
	s_add_i32 s0, s68, 0x2000
	s_cmpk_lg_i32 s68, 0x4000
	s_cselect_b32 s45, s0, 0
	v_add_u32_e32 v160, s70, v230
	ds_read_b64_tr_b16 v[156:157], v160 offset:24576
	ds_read_b64_tr_b16 v[158:159], v160 offset:25088
	v_mfma_f32_32x32x16_f16 v[80:95], v[188:191], v[128:131], v[80:95]
	v_add_f32_e32 v132, v48, v49
	v_add_f32_e32 v132, v50, v132
	v_add_f32_e32 v132, v51, v132
	v_add_f32_e32 v132, v52, v132
	v_add_f32_e32 v132, v53, v132
	v_cvt_pk_f16_f32 v144, v48, v49
	v_cvt_pk_f16_f32 v145, v50, v51
	ds_read_b64_tr_b16 v[152:153], v160 offset:28672
	ds_read_b64_tr_b16 v[154:155], v160 offset:29184
	v_mfma_f32_32x32x16_f16 v[64:79], v[148:151], v[128:131], v[64:79]
	v_add_f32_e32 v48, v54, v132
	v_add_f32_e32 v48, v55, v48
	v_add_f32_e32 v48, v56, v48
	v_add_f32_e32 v48, v57, v48
	v_cvt_pk_f16_f32 v146, v52, v53
	v_cvt_pk_f16_f32 v147, v54, v55
	ds_read_b64_tr_b16 v[148:149], v160 offset:25600
	ds_read_b64_tr_b16 v[150:151], v160 offset:26112
	v_mfma_f32_32x32x16_f16 v[80:95], v[184:187], v[124:127], v[80:95]
	v_add_f32_e32 v48, v58, v48
	v_add_f32_e32 v48, v59, v48
	v_add_f32_e32 v48, v60, v48
	v_add_f32_e32 v48, v61, v48
	v_cvt_pk_f16_f32 v140, v56, v57
	v_cvt_pk_f16_f32 v141, v58, v59
	ds_read_b64_tr_b16 v[52:53], v160 offset:29696
	ds_read_b64_tr_b16 v[54:55], v160 offset:30208
	v_mfma_f32_32x32x16_f16 v[64:79], v[172:175], v[124:127], v[64:79]
	v_add_f32_e32 v48, v62, v48
	v_add_f32_e32 v48, v63, v48
	v_add_f32_e32 v48, v32, v48
	v_add_f32_e32 v56, v33, v48
	v_cvt_pk_f16_f32 v142, v60, v61
	v_cvt_pk_f16_f32 v143, v62, v63
	ds_read_b64_tr_b16 v[48:49], v160 offset:26624
	ds_read_b64_tr_b16 v[50:51], v160 offset:27136
	s_waitcnt lgkmcnt(13)
	v_mfma_f32_32x32x16_f16 v[80:95], v[176:179], v[120:123], v[80:95]
	v_add_f32_e32 v56, v34, v56
	v_add_f32_e32 v56, v35, v56
	v_add_f32_e32 v56, v36, v56
	v_add_f32_e32 v56, v37, v56
	v_cvt_pk_f16_f32 v136, v32, v33
	v_cvt_pk_f16_f32 v137, v34, v35
	ds_read_b64_tr_b16 v[184:185], v160 offset:30720
	ds_read_b64_tr_b16 v[186:187], v160 offset:31232
	s_waitcnt lgkmcnt(14)
	v_mfma_f32_32x32x16_f16 v[64:79], v[164:167], v[120:123], v[64:79]
	v_add_f32_e32 v32, v38, v56
	v_add_f32_e32 v32, v39, v32
	v_add_f32_e32 v32, v40, v32
	v_add_f32_e32 v56, v41, v32
	v_cvt_pk_f16_f32 v138, v36, v37
	v_cvt_pk_f16_f32 v139, v38, v39
	ds_read_b64_tr_b16 v[32:33], v160 offset:27648
	ds_read_b64_tr_b16 v[34:35], v160 offset:28160
	s_waitcnt lgkmcnt(14)
	v_mfma_f32_32x32x16_f16 v[80:95], v[180:183], v[116:119], v[80:95]
	v_add_f32_e32 v36, v42, v56
	v_add_f32_e32 v36, v43, v36
	v_add_f32_e32 v36, v44, v36
	v_add_f32_e32 v36, v45, v36
	v_cvt_pk_f16_f32 v132, v40, v41
	v_cvt_pk_f16_f32 v133, v42, v43
	ds_read_b64_tr_b16 v[180:181], v160 offset:31744
	ds_read_b64_tr_b16 v[182:183], v160 offset:32256
	v_mfma_f32_32x32x16_f16 v[64:79], v[168:171], v[116:119], v[64:79]
	v_add_f32_e32 v36, v46, v36
	v_add_f32_e32 v36, v47, v36
	v_add_f32_e32 v36, 0, v36
	v_cvt_pk_f16_f32 v134, v44, v45
	v_cvt_pk_f16_f32 v135, v46, v47
	s_add_i32 s0, s68, s89
	v_lshl_add_u64 v[38:39], v[194:195], 0, s[30:31]
	s_mov_b32 s1, m0
	s_mov_b32 m0, s0
	s_nop 0
	global_load_lds_dwordx4 v[38:39], off
	s_mov_b32 m0, s1
	s_cmp_lt_u32 s69, 2
	s_cselect_b64 s[0:1], -1, 0
	s_and_b64 s[18:19], s[0:1], exec
	s_cselect_b32 s18, s51, -2
	s_add_i32 s18, s18, s69
	v_mad_i64_i32 v[38:39], s[46:47], s18, v249, v[216:217]
	s_add_i32 s19, s45, s36
	s_mov_b32 s46, m0
	s_mov_b32 m0, s19
	s_nop 0
	global_load_lds_dwordx4 v[38:39], off
	s_mov_b32 m0, s46
	s_andn2_b64 vcc, exec, s[40:41]
	s_cbranch_vccnz .LBB0_484
	s_mov_b64 s[100:101], exec
	v_sub_u32_e32 v38, v215, v197
	v_add_u32_e32 v38, 59, v38
	v_cmpx_gt_i32_e32 59, v38
	s_nop 3
	s_cbranch_execz .Lmaskx_done_8
	v_mov_b32_e32 v79, v248
	v_cmpx_gt_i32_e32 58, v38
	v_mov_b32_e32 v78, v248
	v_cmpx_gt_i32_e32 57, v38
	v_mov_b32_e32 v77, v248
	v_cmpx_gt_i32_e32 56, v38
	v_mov_b32_e32 v76, v248
	v_cmpx_gt_i32_e32 51, v38
	v_mov_b32_e32 v75, v248
	v_cmpx_gt_i32_e32 50, v38
	v_mov_b32_e32 v74, v248
	v_cmpx_gt_i32_e32 49, v38
	v_mov_b32_e32 v73, v248
	v_cmpx_gt_i32_e32 48, v38
	v_mov_b32_e32 v72, v248
	v_cmpx_gt_i32_e32 43, v38
	v_mov_b32_e32 v71, v248
	v_cmpx_gt_i32_e32 42, v38
	v_mov_b32_e32 v70, v248
	v_cmpx_gt_i32_e32 41, v38
	v_mov_b32_e32 v69, v248
	v_cmpx_gt_i32_e32 40, v38
	v_mov_b32_e32 v68, v248
	v_cmpx_gt_i32_e32 35, v38
	v_mov_b32_e32 v67, v248
	v_cmpx_gt_i32_e32 34, v38
	v_mov_b32_e32 v66, v248
	v_cmpx_gt_i32_e32 33, v38
	v_mov_b32_e32 v65, v248
	v_cmpx_gt_i32_e32 32, v38
	v_mov_b32_e32 v64, v248
	v_cmpx_gt_i32_e32 27, v38
	v_mov_b32_e32 v95, v248
	v_cmpx_gt_i32_e32 26, v38
	v_mov_b32_e32 v94, v248
	v_cmpx_gt_i32_e32 25, v38
	v_mov_b32_e32 v93, v248
	v_cmpx_gt_i32_e32 24, v38
	v_mov_b32_e32 v92, v248
	v_cmpx_gt_i32_e32 19, v38
	v_mov_b32_e32 v91, v248
	v_cmpx_gt_i32_e32 18, v38
	v_mov_b32_e32 v90, v248
	v_cmpx_gt_i32_e32 17, v38
	v_mov_b32_e32 v89, v248
	v_cmpx_gt_i32_e32 16, v38
	v_mov_b32_e32 v88, v248
	v_cmpx_gt_i32_e32 11, v38
	v_mov_b32_e32 v87, v248
	v_cmpx_gt_i32_e32 10, v38
	v_mov_b32_e32 v86, v248
	v_cmpx_gt_i32_e32 9, v38
	v_mov_b32_e32 v85, v248
	v_cmpx_gt_i32_e32 8, v38
	v_mov_b32_e32 v84, v248
	v_cmpx_gt_i32_e32 3, v38
	v_mov_b32_e32 v83, v248
	v_cmpx_gt_i32_e32 2, v38
	v_mov_b32_e32 v82, v248
	v_cmpx_gt_i32_e32 1, v38
	v_mov_b32_e32 v81, v248
	v_cmpx_gt_i32_e32 0, v38
	v_mov_b32_e32 v80, v248

; __device__ __forceinline__ void cmask(f32x16& p0, f32x16& p1, int jb, int qrel, int hi) {
;     const float NEG = -INFINITY; int kb = 64 * jb + 4 * hi;
; #pragma unroll
;     for (int r = 0; r < 16; ++r) { int kv = kb + (r & 3) + 8 * (r >> 2); if (kv > qrel) p0[r] = NEG; if (kv + 32 > qrel) p1[r] = NEG; }
; }
.LBB0_500:
	s_add_i32 s68, s26, s19
	s_add_i32 s0, s68, 1
	v_mov_b32_e32 v68, s0
	v_sub_co_u32_e64 v70, s[40:41], s19, 3
	s_nop 1
	v_cndmask_b32_e64 v68, v70, v68, s[40:41]
	v_mad_i64_i32 v[70:71], s[0:1], v68, s48, v[216:217]
	s_add_i32 s0, s18, s36
	s_mov_b32 s1, m0
	s_mov_b32 m0, s0
	s_nop 0
	global_load_lds_dwordx4 v[70:71], off
	s_mov_b32 m0, s1
	s_cmp_gt_u32 s19, 3
	s_cbranch_scc1 .LBB0_502
	s_mov_b64 s[100:101], exec
	v_sub_u32_e32 v71, v215, v237
	v_add_u32_e32 v71, 0x7b, v71
	v_cmpx_gt_i32_e32 59, v71
	s_nop 3
	s_cbranch_execz .Lmaskx_done_7
	v_mov_b32_e32 v47, v248
	v_cmpx_gt_i32_e32 58, v71
	v_mov_b32_e32 v46, v248
	v_cmpx_gt_i32_e32 57, v71
	v_mov_b32_e32 v45, v248
	v_cmpx_gt_i32_e32 56, v71
	v_mov_b32_e32 v44, v248
	v_cmpx_gt_i32_e32 51, v71
	v_mov_b32_e32 v43, v248
	v_cmpx_gt_i32_e32 50, v71
	v_mov_b32_e32 v42, v248
	v_cmpx_gt_i32_e32 49, v71
	v_mov_b32_e32 v41, v248
	v_cmpx_gt_i32_e32 48, v71
	v_mov_b32_e32 v40, v248
	v_cmpx_gt_i32_e32 43, v71
	v_mov_b32_e32 v39, v248
	v_cmpx_gt_i32_e32 42, v71
	v_mov_b32_e32 v38, v248
	v_cmpx_gt_i32_e32 41, v71
	v_mov_b32_e32 v37, v248
	v_cmpx_gt_i32_e32 40, v71
	v_mov_b32_e32 v36, v248
	v_cmpx_gt_i32_e32 35, v71
	v_mov_b32_e32 v35, v248
	v_cmpx_gt_i32_e32 34, v71
	v_mov_b32_e32 v34, v248
	v_cmpx_gt_i32_e32 33, v71
	v_mov_b32_e32 v33, v248
	v_cmpx_gt_i32_e32 32, v71
	v_mov_b32_e32 v32, v248
	v_cmpx_gt_i32_e32 27, v71
	v_mov_b32_e32 v63, v248
	v_cmpx_gt_i32_e32 26, v71
	v_mov_b32_e32 v62, v248
	v_cmpx_gt_i32_e32 25, v71
	v_mov_b32_e32 v61, v248
	v_cmpx_gt_i32_e32 24, v71
	v_mov_b32_e32 v60, v248
	v_cmpx_gt_i32_e32 19, v71
	v_mov_b32_e32 v59, v248
	v_cmpx_gt_i32_e32 18, v71
	v_mov_b32_e32 v58, v248
	v_cmpx_gt_i32_e32 17, v71
	v_mov_b32_e32 v57, v248
	v_cmpx_gt_i32_e32 16, v71
	v_mov_b32_e32 v56, v248
	v_cmpx_gt_i32_e32 11, v71
	v_mov_b32_e32 v55, v248
	v_cmpx_gt_i32_e32 10, v71
	v_mov_b32_e32 v54, v248
	v_cmpx_gt_i32_e32 9, v71
	v_mov_b32_e32 v53, v248
	v_cmpx_gt_i32_e32 8, v71
	v_mov_b32_e32 v52, v248
	v_cmpx_gt_i32_e32 3, v71
	v_mov_b32_e32 v51, v248
	v_cmpx_gt_i32_e32 2, v71
	v_mov_b32_e32 v50, v248
	v_cmpx_gt_i32_e32 1, v71
	v_mov_b32_e32 v49, v248
	v_cmpx_gt_i32_e32 0, v71
	v_mov_b32_e32 v48, v248

; __device__ __forceinline__ void cmask(f32x16& p0, f32x16& p1, int jb, int qrel, int hi) {
;     const float NEG = -INFINITY; int kb = 64 * jb + 4 * hi;
; #pragma unroll
;     for (int r = 0; r < 16; ++r) { int kv = kb + (r & 3) + 8 * (r >> 2); if (kv > qrel) p0[r] = NEG; if (kv + 32 > qrel) p1[r] = NEG; }
; }
.LBB0_511:
	s_andn2_b64 vcc, exec, s[40:41]
	s_cbranch_vccnz .LBB0_513
	s_mov_b64 s[100:101], exec
	v_sub_u32_e32 v240, v215, v237
	v_add_u32_e32 v240, 59, v240
	v_cmpx_gt_i32_e32 59, v240
	s_nop 3
	s_cbranch_execz .Lmaskx_done_6
	v_mov_b32_e32 v79, v248
	v_cmpx_gt_i32_e32 58, v240
	v_mov_b32_e32 v78, v248
	v_cmpx_gt_i32_e32 57, v240
	v_mov_b32_e32 v77, v248
	v_cmpx_gt_i32_e32 56, v240
	v_mov_b32_e32 v76, v248
	v_cmpx_gt_i32_e32 51, v240
	v_mov_b32_e32 v75, v248
	v_cmpx_gt_i32_e32 50, v240
	v_mov_b32_e32 v74, v248
	v_cmpx_gt_i32_e32 49, v240
	v_mov_b32_e32 v73, v248
	v_cmpx_gt_i32_e32 48, v240
	v_mov_b32_e32 v72, v248
	v_cmpx_gt_i32_e32 43, v240
	v_mov_b32_e32 v71, v248
	v_cmpx_gt_i32_e32 42, v240
	v_mov_b32_e32 v70, v248
	v_cmpx_gt_i32_e32 41, v240
	v_mov_b32_e32 v69, v248
	v_cmpx_gt_i32_e32 40, v240
	v_mov_b32_e32 v68, v248
	v_cmpx_gt_i32_e32 35, v240
	v_mov_b32_e32 v67, v248
	v_cmpx_gt_i32_e32 34, v240
	v_mov_b32_e32 v66, v248
	v_cmpx_gt_i32_e32 33, v240
	v_mov_b32_e32 v65, v248
	v_cmpx_gt_i32_e32 32, v240
	v_mov_b32_e32 v64, v248
	v_cmpx_gt_i32_e32 27, v240
	v_mov_b32_e32 v95, v248
	v_cmpx_gt_i32_e32 26, v240
	v_mov_b32_e32 v94, v248
	v_cmpx_gt_i32_e32 25, v240
	v_mov_b32_e32 v93, v248
	v_cmpx_gt_i32_e32 24, v240
	v_mov_b32_e32 v92, v248
	v_cmpx_gt_i32_e32 19, v240
	v_mov_b32_e32 v91, v248
	v_cmpx_gt_i32_e32 18, v240
	v_mov_b32_e32 v90, v248
	v_cmpx_gt_i32_e32 17, v240
	v_mov_b32_e32 v89, v248
	v_cmpx_gt_i32_e32 16, v240
	v_mov_b32_e32 v88, v248
	v_cmpx_gt_i32_e32 11, v240
	v_mov_b32_e32 v87, v248
	v_cmpx_gt_i32_e32 10, v240
	v_mov_b32_e32 v86, v248
	v_cmpx_gt_i32_e32 9, v240
	v_mov_b32_e32 v85, v248
	v_cmpx_gt_i32_e32 8, v240
	v_mov_b32_e32 v84, v248
	v_cmpx_gt_i32_e32 3, v240
	v_mov_b32_e32 v83, v248
	v_cmpx_gt_i32_e32 2, v240
	v_mov_b32_e32 v82, v248
	v_cmpx_gt_i32_e32 1, v240
	v_mov_b32_e32 v81, v248
	v_cmpx_gt_i32_e32 0, v240
	v_mov_b32_e32 v80, v248

; __device__ __forceinline__ void cmask(f32x16& p0, f32x16& p1, int jb, int qrel, int hi) {
;     const float NEG = -INFINITY; int kb = 64 * jb + 4 * hi;
; #pragma unroll
;     for (int r = 0; r < 16; ++r) { int kv = kb + (r & 3) + 8 * (r >> 2); if (kv > qrel) p0[r] = NEG; if (kv + 32 > qrel) p1[r] = NEG; }
; }
.LBB0_565:
	v_add_u32_e32 v184, s18, v230
	ds_read_b64_tr_b16 v[180:181], v184 offset:24576
	ds_read_b64_tr_b16 v[182:183], v184 offset:25088
	s_waitcnt lgkmcnt(9)
	v_mfma_f32_32x32x16_f16 v[48:63], v[176:179], v[128:131], v[48:63]
	v_add_f32_e32 v132, v80, v81
	v_add_f32_e32 v132, v82, v132
	v_add_f32_e32 v132, v83, v132
	v_add_f32_e32 v132, v84, v132
	v_add_f32_e32 v132, v85, v132
	v_cvt_pk_f16_f32 v144, v80, v81
	v_cvt_pk_f16_f32 v145, v82, v83
	ds_read_b64_tr_b16 v[80:81], v184 offset:28672
	ds_read_b64_tr_b16 v[82:83], v184 offset:29184
	s_waitcnt lgkmcnt(10)
	v_mfma_f32_32x32x16_f16 v[32:47], v[172:175], v[128:131], v[32:47]
	v_add_f32_e32 v128, v86, v132
	v_add_f32_e32 v128, v87, v128
	v_add_f32_e32 v128, v88, v128
	v_add_f32_e32 v128, v89, v128
	v_cvt_pk_f16_f32 v146, v84, v85
	v_cvt_pk_f16_f32 v147, v86, v87
	ds_read_b64_tr_b16 v[84:85], v184 offset:25600
	ds_read_b64_tr_b16 v[86:87], v184 offset:26112
	s_waitcnt lgkmcnt(11)
	v_mfma_f32_32x32x16_f16 v[48:63], v[168:171], v[124:127], v[48:63]
	v_add_f32_e32 v128, v90, v128
	v_add_f32_e32 v128, v91, v128
	v_add_f32_e32 v128, v92, v128
	v_add_f32_e32 v128, v93, v128
	v_cvt_pk_f16_f32 v140, v88, v89
	v_cvt_pk_f16_f32 v141, v90, v91
	ds_read_b64_tr_b16 v[88:89], v184 offset:29696
	ds_read_b64_tr_b16 v[90:91], v184 offset:30208
	s_waitcnt lgkmcnt(12)
	v_mfma_f32_32x32x16_f16 v[32:47], v[164:167], v[124:127], v[32:47]
	v_add_f32_e32 v124, v94, v128
	v_add_f32_e32 v124, v95, v124
	v_add_f32_e32 v124, v64, v124
	v_add_f32_e32 v124, v65, v124
	v_cvt_pk_f16_f32 v142, v92, v93
	v_cvt_pk_f16_f32 v143, v94, v95
	ds_read_b64_tr_b16 v[92:93], v184 offset:26624
	ds_read_b64_tr_b16 v[94:95], v184 offset:27136
	s_waitcnt lgkmcnt(13)
	v_mfma_f32_32x32x16_f16 v[48:63], v[160:163], v[120:123], v[48:63]
	v_add_f32_e32 v124, v66, v124
	v_add_f32_e32 v124, v67, v124
	v_add_f32_e32 v124, v68, v124
	v_add_f32_e32 v124, v69, v124
	v_cvt_pk_f16_f32 v136, v64, v65
	v_cvt_pk_f16_f32 v137, v66, v67
	ds_read_b64_tr_b16 v[64:65], v184 offset:30720
	ds_read_b64_tr_b16 v[66:67], v184 offset:31232
	s_waitcnt lgkmcnt(14)
	v_mfma_f32_32x32x16_f16 v[32:47], v[152:155], v[120:123], v[32:47]
	v_add_f32_e32 v120, v70, v124
	v_add_f32_e32 v120, v71, v120
	v_add_f32_e32 v120, v72, v120
	v_add_f32_e32 v120, v73, v120
	v_cvt_pk_f16_f32 v138, v68, v69
	v_cvt_pk_f16_f32 v139, v70, v71
	ds_read_b64_tr_b16 v[68:69], v184 offset:27648
	ds_read_b64_tr_b16 v[70:71], v184 offset:28160
	s_waitcnt lgkmcnt(14)
	v_mfma_f32_32x32x16_f16 v[48:63], v[156:159], v[116:119], v[48:63]
	v_add_f32_e32 v120, v74, v120
	v_add_f32_e32 v120, v75, v120
	v_add_f32_e32 v120, v76, v120
	v_add_f32_e32 v120, v77, v120
	v_cvt_pk_f16_f32 v132, v72, v73
	v_cvt_pk_f16_f32 v133, v74, v75
	ds_read_b64_tr_b16 v[72:73], v184 offset:31744
	ds_read_b64_tr_b16 v[74:75], v184 offset:32256
	v_mfma_f32_32x32x16_f16 v[32:47], v[148:151], v[116:119], v[32:47]
	v_add_f32_e32 v116, v78, v120
	v_add_f32_e32 v116, v79, v116
	v_add_f32_e32 v116, 0, v116
	v_cvt_pk_f16_f32 v134, v76, v77
	v_cvt_pk_f16_f32 v135, v78, v79
	s_andn2_b64 vcc, exec, s[42:43]
	s_cbranch_vccnz .LBB0_567
	s_mov_b64 s[100:101], exec
	v_sub_u32_e32 v77, v215, v233
	v_add_u32_e32 v77, 0xffffff40, v77
	v_cmpx_gt_i32_e32 59, v77
	s_nop 3
	s_cbranch_execz .Lmaskx_done_5
	v_mov_b32_e32 v47, v248
	v_cmpx_gt_i32_e32 58, v77
	v_mov_b32_e32 v46, v248
	v_cmpx_gt_i32_e32 57, v77
	v_mov_b32_e32 v45, v248
	v_cmpx_gt_i32_e32 56, v77
	v_mov_b32_e32 v44, v248
	v_cmpx_gt_i32_e32 51, v77
	v_mov_b32_e32 v43, v248
	v_cmpx_gt_i32_e32 50, v77
	v_mov_b32_e32 v42, v248
	v_cmpx_gt_i32_e32 49, v77
	v_mov_b32_e32 v41, v248
	v_cmpx_gt_i32_e32 48, v77
	v_mov_b32_e32 v40, v248
	v_cmpx_gt_i32_e32 43, v77
	v_mov_b32_e32 v39, v248
	v_cmpx_gt_i32_e32 42, v77
	v_mov_b32_e32 v38, v248
	v_cmpx_gt_i32_e32 41, v77
	v_mov_b32_e32 v37, v248
	v_cmpx_gt_i32_e32 40, v77
	v_mov_b32_e32 v36, v248
	v_cmpx_gt_i32_e32 35, v77
	v_mov_b32_e32 v35, v248
	v_cmpx_gt_i32_e32 34, v77
	v_mov_b32_e32 v34, v248
	v_cmpx_gt_i32_e32 33, v77
	v_mov_b32_e32 v33, v248
	v_cmpx_gt_i32_e32 32, v77
	v_mov_b32_e32 v32, v248
	v_cmpx_gt_i32_e32 27, v77
	v_mov_b32_e32 v63, v248
	v_cmpx_gt_i32_e32 26, v77
	v_mov_b32_e32 v62, v248
	v_cmpx_gt_i32_e32 25, v77
	v_mov_b32_e32 v61, v248
	v_cmpx_gt_i32_e32 24, v77
	v_mov_b32_e32 v60, v248
	v_cmpx_gt_i32_e32 19, v77
	v_mov_b32_e32 v59, v248
	v_cmpx_gt_i32_e32 18, v77
	v_mov_b32_e32 v58, v248
	v_cmpx_gt_i32_e32 17, v77
	v_mov_b32_e32 v57, v248
	v_cmpx_gt_i32_e32 16, v77
	v_mov_b32_e32 v56, v248
	v_cmpx_gt_i32_e32 11, v77
	v_mov_b32_e32 v55, v248
	v_cmpx_gt_i32_e32 10, v77
	v_mov_b32_e32 v54, v248
	v_cmpx_gt_i32_e32 9, v77
	v_mov_b32_e32 v53, v248
	v_cmpx_gt_i32_e32 8, v77
	v_mov_b32_e32 v52, v248
	v_cmpx_gt_i32_e32 3, v77
	v_mov_b32_e32 v51, v248
	v_cmpx_gt_i32_e32 2, v77
	v_mov_b32_e32 v50, v248
	v_cmpx_gt_i32_e32 1, v77
	v_mov_b32_e32 v49, v248
	v_cmpx_gt_i32_e32 0, v77
	v_mov_b32_e32 v48, v248

; __device__ __forceinline__ void cmask(f32x16& p0, f32x16& p1, int jb, int qrel, int hi) {
;     const float NEG = -INFINITY; int kb = 64 * jb + 4 * hi;
; #pragma unroll
;     for (int r = 0; r < 16; ++r) { int kv = kb + (r & 3) + 8 * (r >> 2); if (kv > qrel) p0[r] = NEG; if (kv + 32 > qrel) p1[r] = NEG; }
; }
.LBB0_625:
	v_add_u32_e32 v184, s40, v229
	ds_read_b64_tr_b16 v[180:181], v184 offset:24576
	ds_read_b64_tr_b16 v[182:183], v184 offset:25088
	s_waitcnt lgkmcnt(9)
	v_mfma_f32_32x32x16_f16 v[48:63], v[176:179], v[128:131], v[48:63]
	v_add_f32_e32 v132, v80, v81
	v_add_f32_e32 v132, v82, v132
	v_add_f32_e32 v132, v83, v132
	v_add_f32_e32 v132, v84, v132
	v_add_f32_e32 v132, v85, v132
	v_cvt_pk_f16_f32 v144, v80, v81
	v_cvt_pk_f16_f32 v145, v82, v83
	ds_read_b64_tr_b16 v[176:177], v184 offset:28672
	ds_read_b64_tr_b16 v[178:179], v184 offset:29184
	s_waitcnt lgkmcnt(10)
	v_mfma_f32_32x32x16_f16 v[32:47], v[172:175], v[128:131], v[32:47]
	v_add_f32_e32 v80, v86, v132
	v_add_f32_e32 v80, v87, v80
	v_add_f32_e32 v80, v88, v80
	v_add_f32_e32 v80, v89, v80
	v_cvt_pk_f16_f32 v146, v84, v85
	v_cvt_pk_f16_f32 v147, v86, v87
	ds_read_b64_tr_b16 v[172:173], v184 offset:25600
	ds_read_b64_tr_b16 v[174:175], v184 offset:26112
	s_waitcnt lgkmcnt(11)
	v_mfma_f32_32x32x16_f16 v[48:63], v[168:171], v[124:127], v[48:63]
	v_add_f32_e32 v80, v90, v80
	v_add_f32_e32 v80, v91, v80
	v_add_f32_e32 v80, v92, v80
	v_add_f32_e32 v80, v93, v80
	v_cvt_pk_f16_f32 v140, v88, v89
	v_cvt_pk_f16_f32 v141, v90, v91
	ds_read_b64_tr_b16 v[84:85], v184 offset:29696
	ds_read_b64_tr_b16 v[86:87], v184 offset:30208
	s_waitcnt lgkmcnt(12)
	v_mfma_f32_32x32x16_f16 v[32:47], v[164:167], v[124:127], v[32:47]
	v_add_f32_e32 v80, v94, v80
	v_add_f32_e32 v80, v95, v80
	v_add_f32_e32 v80, v64, v80
	v_add_f32_e32 v88, v65, v80
	v_cvt_pk_f16_f32 v142, v92, v93
	v_cvt_pk_f16_f32 v143, v94, v95
	ds_read_b64_tr_b16 v[80:81], v184 offset:26624
	ds_read_b64_tr_b16 v[82:83], v184 offset:27136
	s_waitcnt lgkmcnt(13)
	v_mfma_f32_32x32x16_f16 v[48:63], v[160:163], v[120:123], v[48:63]
	v_add_f32_e32 v88, v66, v88
	v_add_f32_e32 v88, v67, v88
	v_add_f32_e32 v88, v68, v88
	v_add_f32_e32 v88, v69, v88
	v_cvt_pk_f16_f32 v136, v64, v65
	v_cvt_pk_f16_f32 v137, v66, v67
	ds_read_b64_tr_b16 v[160:161], v184 offset:30720
	ds_read_b64_tr_b16 v[162:163], v184 offset:31232
	s_waitcnt lgkmcnt(14)
	v_mfma_f32_32x32x16_f16 v[32:47], v[152:155], v[120:123], v[32:47]
	v_add_f32_e32 v64, v70, v88
	v_add_f32_e32 v64, v71, v64
	v_add_f32_e32 v64, v72, v64
	v_add_f32_e32 v88, v73, v64
	v_cvt_pk_f16_f32 v138, v68, v69
	v_cvt_pk_f16_f32 v139, v70, v71
	ds_read_b64_tr_b16 v[64:65], v184 offset:27648
	ds_read_b64_tr_b16 v[66:67], v184 offset:28160
	s_waitcnt lgkmcnt(14)
	v_mfma_f32_32x32x16_f16 v[48:63], v[156:159], v[116:119], v[48:63]
	v_add_f32_e32 v68, v74, v88
	v_add_f32_e32 v68, v75, v68
	v_add_f32_e32 v68, v76, v68
	v_add_f32_e32 v68, v77, v68
	v_cvt_pk_f16_f32 v132, v72, v73
	v_cvt_pk_f16_f32 v133, v74, v75
	ds_read_b64_tr_b16 v[152:153], v184 offset:31744
	ds_read_b64_tr_b16 v[154:155], v184 offset:32256
	v_mfma_f32_32x32x16_f16 v[32:47], v[148:151], v[116:119], v[32:47]
	v_add_f32_e32 v68, v78, v68
	v_add_f32_e32 v68, v79, v68
	v_add_f32_e32 v68, 0, v68
	v_cvt_pk_f16_f32 v134, v76, v77
	v_cvt_pk_f16_f32 v135, v78, v79
	v_lshl_add_u64 v[70:71], v[194:195], 0, s[30:31]
	s_add_i32 s11, s69, s90
	s_mov_b32 s18, m0
	s_mov_b32 m0, s11
	s_nop 0
	global_load_lds_dwordx4 v[70:71], off
	s_mov_b32 m0, s18
	s_add_i32 s18, s26, s45
	s_add_i32 s37, s26, s19
	s_add_i32 s11, s18, 1
	s_add_i32 s66, s37, 1
	s_cmp_lt_u32 s45, 3
	s_cselect_b64 s[40:41], -1, 0
	s_and_b64 s[50:51], s[40:41], exec
	s_cselect_b32 s11, s11, s66
	v_mad_i64_i32 v[70:71], s[50:51], s11, v249, v[216:217]
	s_add_i32 s50, s68, s10
	s_mov_b32 s51, m0
	s_mov_b32 m0, s50
	s_nop 0
	global_load_lds_dwordx4 v[70:71], off
	s_mov_b32 m0, s51
	s_cmp_gt_u32 s45, 3
	s_cbranch_scc1 .LBB0_627
	s_mov_b64 s[100:101], exec
	v_sub_u32_e32 v69, v215, v196
	v_add_u32_e32 v69, 32, v69
	v_cmpx_gt_i32_e32 59, v69
	s_nop 3
	s_cbranch_execz .Lmaskx_done_4
	v_mov_b32_e32 v47, v248
	v_cmpx_gt_i32_e32 58, v69
	v_mov_b32_e32 v46, v248
	v_cmpx_gt_i32_e32 57, v69
	v_mov_b32_e32 v45, v248
	v_cmpx_gt_i32_e32 56, v69
	v_mov_b32_e32 v44, v248
	v_cmpx_gt_i32_e32 51, v69
	v_mov_b32_e32 v43, v248
	v_cmpx_gt_i32_e32 50, v69
	v_mov_b32_e32 v42, v248
	v_cmpx_gt_i32_e32 49, v69
	v_mov_b32_e32 v41, v248
	v_cmpx_gt_i32_e32 48, v69
	v_mov_b32_e32 v40, v248
	v_cmpx_gt_i32_e32 43, v69
	v_mov_b32_e32 v39, v248
	v_cmpx_gt_i32_e32 42, v69
	v_mov_b32_e32 v38, v248
	v_cmpx_gt_i32_e32 41, v69
	v_mov_b32_e32 v37, v248
	v_cmpx_gt_i32_e32 40, v69
	v_mov_b32_e32 v36, v248
	v_cmpx_gt_i32_e32 35, v69
	v_mov_b32_e32 v35, v248
	v_cmpx_gt_i32_e32 34, v69
	v_mov_b32_e32 v34, v248
	v_cmpx_gt_i32_e32 33, v69
	v_mov_b32_e32 v33, v248
	v_cmpx_gt_i32_e32 32, v69
	v_mov_b32_e32 v32, v248
	v_cmpx_gt_i32_e32 27, v69
	v_mov_b32_e32 v63, v248
	v_cmpx_gt_i32_e32 26, v69
	v_mov_b32_e32 v62, v248
	v_cmpx_gt_i32_e32 25, v69
	v_mov_b32_e32 v61, v248
	v_cmpx_gt_i32_e32 24, v69
	v_mov_b32_e32 v60, v248
	v_cmpx_gt_i32_e32 19, v69
	v_mov_b32_e32 v59, v248
	v_cmpx_gt_i32_e32 18, v69
	v_mov_b32_e32 v58, v248
	v_cmpx_gt_i32_e32 17, v69
	v_mov_b32_e32 v57, v248
	v_cmpx_gt_i32_e32 16, v69
	v_mov_b32_e32 v56, v248
	v_cmpx_gt_i32_e32 11, v69
	v_mov_b32_e32 v55, v248
	v_cmpx_gt_i32_e32 10, v69
	v_mov_b32_e32 v54, v248
	v_cmpx_gt_i32_e32 9, v69
	v_mov_b32_e32 v53, v248
	v_cmpx_gt_i32_e32 8, v69
	v_mov_b32_e32 v52, v248
	v_cmpx_gt_i32_e32 3, v69
	v_mov_b32_e32 v51, v248
	v_cmpx_gt_i32_e32 2, v69
	v_mov_b32_e32 v50, v248
	v_cmpx_gt_i32_e32 1, v69
	v_mov_b32_e32 v49, v248
	v_cmpx_gt_i32_e32 0, v69
	v_mov_b32_e32 v48, v248

; __device__ __forceinline__ void cmask(f32x16& p0, f32x16& p1, int jb, int qrel, int hi) {
;     const float NEG = -INFINITY; int kb = 64 * jb + 4 * hi;
; #pragma unroll
;     for (int r = 0; r < 16; ++r) { int kv = kb + (r & 3) + 8 * (r >> 2); if (kv > qrel) p0[r] = NEG; if (kv + 32 > qrel) p1[r] = NEG; }
; }
.LBB0_630:
	s_add_i32 s11, s68, 0x2000
	s_cmpk_lg_i32 s68, 0x4000
	s_cselect_b32 s11, s11, 0
	v_add_u32_e32 v160, s69, v229
	ds_read_b64_tr_b16 v[156:157], v160 offset:24576
	ds_read_b64_tr_b16 v[158:159], v160 offset:25088
	v_mfma_f32_32x32x16_f16 v[80:95], v[188:191], v[128:131], v[80:95]
	v_add_f32_e32 v132, v48, v49
	v_add_f32_e32 v132, v50, v132
	v_add_f32_e32 v132, v51, v132
	v_add_f32_e32 v132, v52, v132
	v_add_f32_e32 v132, v53, v132
	v_cvt_pk_f16_f32 v144, v48, v49
	v_cvt_pk_f16_f32 v145, v50, v51
	ds_read_b64_tr_b16 v[152:153], v160 offset:28672
	ds_read_b64_tr_b16 v[154:155], v160 offset:29184
	v_mfma_f32_32x32x16_f16 v[64:79], v[148:151], v[128:131], v[64:79]
	v_add_f32_e32 v48, v54, v132
	v_add_f32_e32 v48, v55, v48
	v_add_f32_e32 v48, v56, v48
	v_add_f32_e32 v48, v57, v48
	v_cvt_pk_f16_f32 v146, v52, v53
	v_cvt_pk_f16_f32 v147, v54, v55
	ds_read_b64_tr_b16 v[148:149], v160 offset:25600
	ds_read_b64_tr_b16 v[150:151], v160 offset:26112
	v_mfma_f32_32x32x16_f16 v[80:95], v[184:187], v[124:127], v[80:95]
	v_add_f32_e32 v48, v58, v48
	v_add_f32_e32 v48, v59, v48
	v_add_f32_e32 v48, v60, v48
	v_add_f32_e32 v48, v61, v48
	v_cvt_pk_f16_f32 v140, v56, v57
	v_cvt_pk_f16_f32 v141, v58, v59
	ds_read_b64_tr_b16 v[52:53], v160 offset:29696
	ds_read_b64_tr_b16 v[54:55], v160 offset:30208
	v_mfma_f32_32x32x16_f16 v[64:79], v[172:175], v[124:127], v[64:79]
	v_add_f32_e32 v48, v62, v48
	v_add_f32_e32 v48, v63, v48
	v_add_f32_e32 v48, v32, v48
	v_add_f32_e32 v56, v33, v48
	v_cvt_pk_f16_f32 v142, v60, v61
	v_cvt_pk_f16_f32 v143, v62, v63
	ds_read_b64_tr_b16 v[48:49], v160 offset:26624
	ds_read_b64_tr_b16 v[50:51], v160 offset:27136
	s_waitcnt lgkmcnt(13)
	v_mfma_f32_32x32x16_f16 v[80:95], v[176:179], v[120:123], v[80:95]
	v_add_f32_e32 v56, v34, v56
	v_add_f32_e32 v56, v35, v56
	v_add_f32_e32 v56, v36, v56
	v_add_f32_e32 v56, v37, v56
	v_cvt_pk_f16_f32 v136, v32, v33
	v_cvt_pk_f16_f32 v137, v34, v35
	ds_read_b64_tr_b16 v[184:185], v160 offset:30720
	ds_read_b64_tr_b16 v[186:187], v160 offset:31232
	s_waitcnt lgkmcnt(14)
	v_mfma_f32_32x32x16_f16 v[64:79], v[164:167], v[120:123], v[64:79]
	v_add_f32_e32 v32, v38, v56
	v_add_f32_e32 v32, v39, v32
	v_add_f32_e32 v32, v40, v32
	v_add_f32_e32 v56, v41, v32
	v_cvt_pk_f16_f32 v138, v36, v37
	v_cvt_pk_f16_f32 v139, v38, v39
	ds_read_b64_tr_b16 v[32:33], v160 offset:27648
	ds_read_b64_tr_b16 v[34:35], v160 offset:28160
	s_waitcnt lgkmcnt(14)
	v_mfma_f32_32x32x16_f16 v[80:95], v[180:183], v[116:119], v[80:95]
	v_add_f32_e32 v36, v42, v56
	v_add_f32_e32 v36, v43, v36
	v_add_f32_e32 v36, v44, v36
	v_add_f32_e32 v36, v45, v36
	v_cvt_pk_f16_f32 v132, v40, v41
	v_cvt_pk_f16_f32 v133, v42, v43
	ds_read_b64_tr_b16 v[180:181], v160 offset:31744
	ds_read_b64_tr_b16 v[182:183], v160 offset:32256
	v_mfma_f32_32x32x16_f16 v[64:79], v[168:171], v[116:119], v[64:79]
	v_add_f32_e32 v36, v46, v36
	v_add_f32_e32 v36, v47, v36
	v_add_f32_e32 v36, 0, v36
	v_cvt_pk_f16_f32 v134, v44, v45
	v_cvt_pk_f16_f32 v135, v46, v47
	s_add_i32 s50, s68, s90
	s_add_i32 s18, s18, 2
	s_cmp_lt_u32 s45, 2
	s_mov_b32 s51, m0
	s_mov_b32 m0, s50
	s_nop 0
	global_load_lds_dwordx4 v[194:195], off
	s_mov_b32 m0, s51
	s_cselect_b32 s18, s18, s37
	v_mad_i64_i32 v[38:39], s[50:51], s18, v249, v[216:217]
	s_add_i32 s37, s11, s10
	s_mov_b32 s50, m0
	s_mov_b32 m0, s37
	s_nop 0
	global_load_lds_dwordx4 v[38:39], off
	s_mov_b32 m0, s50
	s_andn2_b64 vcc, exec, s[40:41]
	s_cbranch_vccnz .LBB0_632
	s_mov_b64 s[100:101], exec
	v_sub_u32_e32 v38, v215, v196
	v_add_u32_e32 v38, 0xffffffe0, v38
	v_cmpx_gt_i32_e32 59, v38
	s_nop 3
	s_cbranch_execz .Lmaskx_done_3
	v_mov_b32_e32 v79, v248
	v_cmpx_gt_i32_e32 58, v38
	v_mov_b32_e32 v78, v248
	v_cmpx_gt_i32_e32 57, v38
	v_mov_b32_e32 v77, v248
	v_cmpx_gt_i32_e32 56, v38
	v_mov_b32_e32 v76, v248
	v_cmpx_gt_i32_e32 51, v38
	v_mov_b32_e32 v75, v248
	v_cmpx_gt_i32_e32 50, v38
	v_mov_b32_e32 v74, v248
	v_cmpx_gt_i32_e32 49, v38
	v_mov_b32_e32 v73, v248
	v_cmpx_gt_i32_e32 48, v38
	v_mov_b32_e32 v72, v248
	v_cmpx_gt_i32_e32 43, v38
	v_mov_b32_e32 v71, v248
	v_cmpx_gt_i32_e32 42, v38
	v_mov_b32_e32 v70, v248
	v_cmpx_gt_i32_e32 41, v38
	v_mov_b32_e32 v69, v248
	v_cmpx_gt_i32_e32 40, v38
	v_mov_b32_e32 v68, v248
	v_cmpx_gt_i32_e32 35, v38
	v_mov_b32_e32 v67, v248
	v_cmpx_gt_i32_e32 34, v38
	v_mov_b32_e32 v66, v248
	v_cmpx_gt_i32_e32 33, v38
	v_mov_b32_e32 v65, v248
	v_cmpx_gt_i32_e32 32, v38
	v_mov_b32_e32 v64, v248
	v_cmpx_gt_i32_e32 27, v38
	v_mov_b32_e32 v95, v248
	v_cmpx_gt_i32_e32 26, v38
	v_mov_b32_e32 v94, v248
	v_cmpx_gt_i32_e32 25, v38
	v_mov_b32_e32 v93, v248
	v_cmpx_gt_i32_e32 24, v38
	v_mov_b32_e32 v92, v248
	v_cmpx_gt_i32_e32 19, v38
	v_mov_b32_e32 v91, v248
	v_cmpx_gt_i32_e32 18, v38
	v_mov_b32_e32 v90, v248
	v_cmpx_gt_i32_e32 17, v38
	v_mov_b32_e32 v89, v248
	v_cmpx_gt_i32_e32 16, v38
	v_mov_b32_e32 v88, v248
	v_cmpx_gt_i32_e32 11, v38
	v_mov_b32_e32 v87, v248
	v_cmpx_gt_i32_e32 10, v38
	v_mov_b32_e32 v86, v248
	v_cmpx_gt_i32_e32 9, v38
	v_mov_b32_e32 v85, v248
	v_cmpx_gt_i32_e32 8, v38
	v_mov_b32_e32 v84, v248
	v_cmpx_gt_i32_e32 3, v38
	v_mov_b32_e32 v83, v248
	v_cmpx_gt_i32_e32 2, v38
	v_mov_b32_e32 v82, v248
	v_cmpx_gt_i32_e32 1, v38
	v_mov_b32_e32 v81, v248
	v_cmpx_gt_i32_e32 0, v38
	v_mov_b32_e32 v80, v248

; __device__ __forceinline__ void cmask(f32x16& p0, f32x16& p1, int jb, int qrel, int hi) {
;     const float NEG = -INFINITY; int kb = 64 * jb + 4 * hi;
; #pragma unroll
;     for (int r = 0; r < 16; ++r) { int kv = kb + (r & 3) + 8 * (r >> 2); if (kv > qrel) p0[r] = NEG; if (kv + 32 > qrel) p1[r] = NEG; }
; }
.LBB0_648:
	s_add_i32 s28, s26, s37
	s_add_i32 s45, s28, 1
	s_cmp_lt_u32 s37, 3
	s_cselect_b64 s[40:41], -1, 0
	s_and_b64 s[66:67], s[40:41], exec
	s_cselect_b32 s45, s45, s19
	v_mad_i64_i32 v[70:71], s[66:67], s45, v249, v[216:217]
	s_add_i32 s66, s18, s10
	s_mov_b32 s67, m0
	s_mov_b32 m0, s66
	s_nop 0
	global_load_lds_dwordx4 v[70:71], off
	s_mov_b32 m0, s67
	s_cmp_gt_u32 s37, 3
	s_cbranch_scc1 .LBB0_650
	s_mov_b64 s[100:101], exec
	v_sub_u32_e32 v70, v215, v234
	v_add_u32_e32 v70, 0x7b, v70
	v_cmpx_gt_i32_e32 59, v70
	s_nop 3
	s_cbranch_execz .Lmaskx_done_2
	v_mov_b32_e32 v47, v248
	v_cmpx_gt_i32_e32 58, v70
	v_mov_b32_e32 v46, v248
	v_cmpx_gt_i32_e32 57, v70
	v_mov_b32_e32 v45, v248
	v_cmpx_gt_i32_e32 56, v70
	v_mov_b32_e32 v44, v248
	v_cmpx_gt_i32_e32 51, v70
	v_mov_b32_e32 v43, v248
	v_cmpx_gt_i32_e32 50, v70
	v_mov_b32_e32 v42, v248
	v_cmpx_gt_i32_e32 49, v70
	v_mov_b32_e32 v41, v248
	v_cmpx_gt_i32_e32 48, v70
	v_mov_b32_e32 v40, v248
	v_cmpx_gt_i32_e32 43, v70
	v_mov_b32_e32 v39, v248
	v_cmpx_gt_i32_e32 42, v70
	v_mov_b32_e32 v38, v248
	v_cmpx_gt_i32_e32 41, v70
	v_mov_b32_e32 v37, v248
	v_cmpx_gt_i32_e32 40, v70
	v_mov_b32_e32 v36, v248
	v_cmpx_gt_i32_e32 35, v70
	v_mov_b32_e32 v35, v248
	v_cmpx_gt_i32_e32 34, v70
	v_mov_b32_e32 v34, v248
	v_cmpx_gt_i32_e32 33, v70
	v_mov_b32_e32 v33, v248
	v_cmpx_gt_i32_e32 32, v70
	v_mov_b32_e32 v32, v248
	v_cmpx_gt_i32_e32 27, v70
	v_mov_b32_e32 v63, v248
	v_cmpx_gt_i32_e32 26, v70
	v_mov_b32_e32 v62, v248
	v_cmpx_gt_i32_e32 25, v70
	v_mov_b32_e32 v61, v248
	v_cmpx_gt_i32_e32 24, v70
	v_mov_b32_e32 v60, v248
	v_cmpx_gt_i32_e32 19, v70
	v_mov_b32_e32 v59, v248
	v_cmpx_gt_i32_e32 18, v70
	v_mov_b32_e32 v58, v248
	v_cmpx_gt_i32_e32 17, v70
	v_mov_b32_e32 v57, v248
	v_cmpx_gt_i32_e32 16, v70
	v_mov_b32_e32 v56, v248
	v_cmpx_gt_i32_e32 11, v70
	v_mov_b32_e32 v55, v248
	v_cmpx_gt_i32_e32 10, v70
	v_mov_b32_e32 v54, v248
	v_cmpx_gt_i32_e32 9, v70
	v_mov_b32_e32 v53, v248
	v_cmpx_gt_i32_e32 8, v70
	v_mov_b32_e32 v52, v248
	v_cmpx_gt_i32_e32 3, v70
	v_mov_b32_e32 v51, v248
	v_cmpx_gt_i32_e32 2, v70
	v_mov_b32_e32 v50, v248
	v_cmpx_gt_i32_e32 1, v70
	v_mov_b32_e32 v49, v248
	v_cmpx_gt_i32_e32 0, v70
	v_mov_b32_e32 v48, v248

; __device__ __forceinline__ void cmask(f32x16& p0, f32x16& p1, int jb, int qrel, int hi) {
;     const float NEG = -INFINITY; int kb = 64 * jb + 4 * hi;
; #pragma unroll
;     for (int r = 0; r < 16; ++r) { int kv = kb + (r & 3) + 8 * (r >> 2); if (kv > qrel) p0[r] = NEG; if (kv + 32 > qrel) p1[r] = NEG; }
; }
.LBB0_659:
	s_andn2_b64 vcc, exec, s[40:41]
	s_cbranch_vccnz .LBB0_661
	s_mov_b64 s[100:101], exec
	v_sub_u32_e32 v237, v215, v234
	v_add_u32_e32 v237, 59, v237
	v_cmpx_gt_i32_e32 59, v237
	s_nop 3
	s_cbranch_execz .Lmaskx_done_1
	v_mov_b32_e32 v79, v248
	v_cmpx_gt_i32_e32 58, v237
	v_mov_b32_e32 v78, v248
	v_cmpx_gt_i32_e32 57, v237
	v_mov_b32_e32 v77, v248
	v_cmpx_gt_i32_e32 56, v237
	v_mov_b32_e32 v76, v248
	v_cmpx_gt_i32_e32 51, v237
	v_mov_b32_e32 v75, v248
	v_cmpx_gt_i32_e32 50, v237
	v_mov_b32_e32 v74, v248
	v_cmpx_gt_i32_e32 49, v237
	v_mov_b32_e32 v73, v248
	v_cmpx_gt_i32_e32 48, v237
	v_mov_b32_e32 v72, v248
	v_cmpx_gt_i32_e32 43, v237
	v_mov_b32_e32 v71, v248
	v_cmpx_gt_i32_e32 42, v237
	v_mov_b32_e32 v70, v248
	v_cmpx_gt_i32_e32 41, v237
	v_mov_b32_e32 v69, v248
	v_cmpx_gt_i32_e32 40, v237
	v_mov_b32_e32 v68, v248
	v_cmpx_gt_i32_e32 35, v237
	v_mov_b32_e32 v67, v248
	v_cmpx_gt_i32_e32 34, v237
	v_mov_b32_e32 v66, v248
	v_cmpx_gt_i32_e32 33, v237
	v_mov_b32_e32 v65, v248
	v_cmpx_gt_i32_e32 32, v237
	v_mov_b32_e32 v64, v248
	v_cmpx_gt_i32_e32 27, v237
	v_mov_b32_e32 v95, v248
	v_cmpx_gt_i32_e32 26, v237
	v_mov_b32_e32 v94, v248
	v_cmpx_gt_i32_e32 25, v237
	v_mov_b32_e32 v93, v248
	v_cmpx_gt_i32_e32 24, v237
	v_mov_b32_e32 v92, v248
	v_cmpx_gt_i32_e32 19, v237
	v_mov_b32_e32 v91, v248
	v_cmpx_gt_i32_e32 18, v237
	v_mov_b32_e32 v90, v248
	v_cmpx_gt_i32_e32 17, v237
	v_mov_b32_e32 v89, v248
	v_cmpx_gt_i32_e32 16, v237
	v_mov_b32_e32 v88, v248
	v_cmpx_gt_i32_e32 11, v237
	v_mov_b32_e32 v87, v248
	v_cmpx_gt_i32_e32 10, v237
	v_mov_b32_e32 v86, v248
	v_cmpx_gt_i32_e32 9, v237
	v_mov_b32_e32 v85, v248
	v_cmpx_gt_i32_e32 8, v237
	v_mov_b32_e32 v84, v248
	v_cmpx_gt_i32_e32 3, v237
	v_mov_b32_e32 v83, v248
	v_cmpx_gt_i32_e32 2, v237
	v_mov_b32_e32 v82, v248
	v_cmpx_gt_i32_e32 1, v237
	v_mov_b32_e32 v81, v248
	v_cmpx_gt_i32_e32 0, v237
	v_mov_b32_e32 v80, v248

; __device__ __forceinline__ void cmask(f32x16& p0, f32x16& p1, int jb, int qrel, int hi) {
;     const float NEG = -INFINITY; int kb = 64 * jb + 4 * hi;
; #pragma unroll
;     for (int r = 0; r < 16; ++r) { int kv = kb + (r & 3) + 8 * (r >> 2); if (kv > qrel) p0[r] = NEG; if (kv + 32 > qrel) p1[r] = NEG; }
; }
.LBB0_711:
	v_add_u32_e32 v184, s18, v229
	ds_read_b64_tr_b16 v[180:181], v184 offset:24576
	ds_read_b64_tr_b16 v[182:183], v184 offset:25088
	s_waitcnt lgkmcnt(9)
	v_mfma_f32_32x32x16_f16 v[48:63], v[176:179], v[128:131], v[48:63]
	v_add_f32_e32 v132, v80, v81
	v_add_f32_e32 v132, v82, v132
	v_add_f32_e32 v132, v83, v132
	v_add_f32_e32 v132, v84, v132
	v_add_f32_e32 v132, v85, v132
	v_cvt_pk_f16_f32 v144, v80, v81
	v_cvt_pk_f16_f32 v145, v82, v83
	ds_read_b64_tr_b16 v[80:81], v184 offset:28672
	ds_read_b64_tr_b16 v[82:83], v184 offset:29184
	s_waitcnt lgkmcnt(10)
	v_mfma_f32_32x32x16_f16 v[32:47], v[172:175], v[128:131], v[32:47]
	v_add_f32_e32 v128, v86, v132
	v_add_f32_e32 v128, v87, v128
	v_add_f32_e32 v128, v88, v128
	v_add_f32_e32 v128, v89, v128
	v_cvt_pk_f16_f32 v146, v84, v85
	v_cvt_pk_f16_f32 v147, v86, v87
	ds_read_b64_tr_b16 v[84:85], v184 offset:25600
	ds_read_b64_tr_b16 v[86:87], v184 offset:26112
	s_waitcnt lgkmcnt(11)
	v_mfma_f32_32x32x16_f16 v[48:63], v[168:171], v[124:127], v[48:63]
	v_add_f32_e32 v128, v90, v128
	v_add_f32_e32 v128, v91, v128
	v_add_f32_e32 v128, v92, v128
	v_add_f32_e32 v128, v93, v128
	v_cvt_pk_f16_f32 v140, v88, v89
	v_cvt_pk_f16_f32 v141, v90, v91
	ds_read_b64_tr_b16 v[88:89], v184 offset:29696
	ds_read_b64_tr_b16 v[90:91], v184 offset:30208
	s_waitcnt lgkmcnt(12)
	v_mfma_f32_32x32x16_f16 v[32:47], v[164:167], v[124:127], v[32:47]
	v_add_f32_e32 v124, v94, v128
	v_add_f32_e32 v124, v95, v124
	v_add_f32_e32 v124, v64, v124
	v_add_f32_e32 v124, v65, v124
	v_cvt_pk_f16_f32 v142, v92, v93
	v_cvt_pk_f16_f32 v143, v94, v95
	ds_read_b64_tr_b16 v[92:93], v184 offset:26624
	ds_read_b64_tr_b16 v[94:95], v184 offset:27136
	s_waitcnt lgkmcnt(13)
	v_mfma_f32_32x32x16_f16 v[48:63], v[160:163], v[120:123], v[48:63]
	v_add_f32_e32 v124, v66, v124
	v_add_f32_e32 v124, v67, v124
	v_add_f32_e32 v124, v68, v124
	v_add_f32_e32 v124, v69, v124
	v_cvt_pk_f16_f32 v136, v64, v65
	v_cvt_pk_f16_f32 v137, v66, v67
	ds_read_b64_tr_b16 v[64:65], v184 offset:30720
	ds_read_b64_tr_b16 v[66:67], v184 offset:31232
	s_waitcnt lgkmcnt(14)
	v_mfma_f32_32x32x16_f16 v[32:47], v[152:155], v[120:123], v[32:47]
	v_add_f32_e32 v120, v70, v124
	v_add_f32_e32 v120, v71, v120
	v_add_f32_e32 v120, v72, v120
	v_add_f32_e32 v120, v73, v120
	v_cvt_pk_f16_f32 v138, v68, v69
	v_cvt_pk_f16_f32 v139, v70, v71
	ds_read_b64_tr_b16 v[68:69], v184 offset:27648
	ds_read_b64_tr_b16 v[70:71], v184 offset:28160
	s_waitcnt lgkmcnt(14)
	v_mfma_f32_32x32x16_f16 v[48:63], v[156:159], v[116:119], v[48:63]
	v_add_f32_e32 v120, v74, v120
	v_add_f32_e32 v120, v75, v120
	v_add_f32_e32 v120, v76, v120
	v_add_f32_e32 v120, v77, v120
	v_cvt_pk_f16_f32 v132, v72, v73
	v_cvt_pk_f16_f32 v133, v74, v75
	ds_read_b64_tr_b16 v[72:73], v184 offset:31744
	ds_read_b64_tr_b16 v[74:75], v184 offset:32256
	v_mfma_f32_32x32x16_f16 v[32:47], v[148:151], v[116:119], v[32:47]
	v_add_f32_e32 v116, v78, v120
	v_add_f32_e32 v116, v79, v116
	v_add_f32_e32 v116, 0, v116
	v_cvt_pk_f16_f32 v134, v76, v77
	v_cvt_pk_f16_f32 v135, v78, v79
	s_andn2_b64 vcc, exec, s[0:1]
	s_cbranch_vccnz .LBB0_713
	s_mov_b64 s[100:101], exec
	v_sub_u32_e32 v77, v215, v231
	v_add_u32_e32 v77, 0xffffff40, v77
	v_cmpx_gt_i32_e32 59, v77
	s_nop 3
	s_cbranch_execz .Lmaskx_done_0
	v_mov_b32_e32 v47, v248
	v_cmpx_gt_i32_e32 58, v77
	v_mov_b32_e32 v46, v248
	v_cmpx_gt_i32_e32 57, v77
	v_mov_b32_e32 v45, v248
	v_cmpx_gt_i32_e32 56, v77
	v_mov_b32_e32 v44, v248
	v_cmpx_gt_i32_e32 51, v77
	v_mov_b32_e32 v43, v248
	v_cmpx_gt_i32_e32 50, v77
	v_mov_b32_e32 v42, v248
	v_cmpx_gt_i32_e32 49, v77
	v_mov_b32_e32 v41, v248
	v_cmpx_gt_i32_e32 48, v77
	v_mov_b32_e32 v40, v248
	v_cmpx_gt_i32_e32 43, v77
	v_mov_b32_e32 v39, v248
	v_cmpx_gt_i32_e32 42, v77
	v_mov_b32_e32 v38, v248
	v_cmpx_gt_i32_e32 41, v77
	v_mov_b32_e32 v37, v248
	v_cmpx_gt_i32_e32 40, v77
	v_mov_b32_e32 v36, v248
	v_cmpx_gt_i32_e32 35, v77
	v_mov_b32_e32 v35, v248
	v_cmpx_gt_i32_e32 34, v77
	v_mov_b32_e32 v34, v248
	v_cmpx_gt_i32_e32 33, v77
	v_mov_b32_e32 v33, v248
	v_cmpx_gt_i32_e32 32, v77
	v_mov_b32_e32 v32, v248
	v_cmpx_gt_i32_e32 27, v77
	v_mov_b32_e32 v63, v248
	v_cmpx_gt_i32_e32 26, v77
	v_mov_b32_e32 v62, v248
	v_cmpx_gt_i32_e32 25, v77
	v_mov_b32_e32 v61, v248
	v_cmpx_gt_i32_e32 24, v77
	v_mov_b32_e32 v60, v248
	v_cmpx_gt_i32_e32 19, v77
	v_mov_b32_e32 v59, v248
	v_cmpx_gt_i32_e32 18, v77
	v_mov_b32_e32 v58, v248
	v_cmpx_gt_i32_e32 17, v77
	v_mov_b32_e32 v57, v248
	v_cmpx_gt_i32_e32 16, v77
	v_mov_b32_e32 v56, v248
	v_cmpx_gt_i32_e32 11, v77
	v_mov_b32_e32 v55, v248
	v_cmpx_gt_i32_e32 10, v77
	v_mov_b32_e32 v54, v248
	v_cmpx_gt_i32_e32 9, v77
	v_mov_b32_e32 v53, v248
	v_cmpx_gt_i32_e32 8, v77
	v_mov_b32_e32 v52, v248
	v_cmpx_gt_i32_e32 3, v77
	v_mov_b32_e32 v51, v248
	v_cmpx_gt_i32_e32 2, v77
	v_mov_b32_e32 v50, v248
	v_cmpx_gt_i32_e32 1, v77
	v_mov_b32_e32 v49, v248
	v_cmpx_gt_i32_e32 0, v77
	v_mov_b32_e32 v48, v248
